# baseline (speedup 1.0000x reference)
.LBB0_3:
	s_setprio 3
	s_load_dwordx8 s[8:15], s[0:1], 0x0
	v_and_b32_e32 v199, 15, v0
	v_lshrrev_b32_e32 v206, 4, v1
	s_cmpk_gt_u32 s38, 0x17f
	v_lshlrev_b32_e32 v205, 2, v206
	v_lshlrev_b32_e32 v194, 4, v206
	s_mul_i32 s37, s3, 0xc8
	v_lshl_or_b32 v204, s36, 4, v199
	s_cbranch_scc0 .LBB0_52
	s_add_i32 s39, s36, -6
	s_lshl_b32 s4, s33, 7
	s_waitcnt lgkmcnt(0)
	s_add_u32 s40, s20, s4
	s_addc_u32 s41, s21, 0
	s_add_u32 s6, s24, s4
	s_addc_u32 s7, s25, 0
	s_lshl_b32 s24, s39, 4
	v_or_b32_e32 v131, s24, v199
	v_min_u32_e32 v2, 0xc7, v131
	v_add_u32_e32 v2, s37, v2
	v_ashrrev_i32_e32 v3, 31, v2
	v_lshlrev_b64 v[2:3], 2, v[2:3]
	s_add_i32 s21, s36, -4
	v_lshl_add_u64 v[4:5], s[8:9], 0, v[2:3]
	v_lshl_add_u64 v[2:3], s[10:11], 0, v[2:3]
	v_lshl_or_b32 v201, s21, 4, v199
	global_load_dword v35, v[2:3], off
	v_min_u32_e32 v2, 0xc7, v201
	v_add_u32_e32 v2, s37, v2
	v_ashrrev_i32_e32 v3, 31, v2
	v_lshlrev_b64 v[2:3], 2, v[2:3]
	global_load_dword v34, v[4:5], off
	v_lshl_add_u64 v[4:5], s[8:9], 0, v[2:3]
	v_lshl_add_u64 v[2:3], s[10:11], 0, v[2:3]
	global_load_dword v36, v[4:5], off
	global_load_dword v37, v[2:3], off
	v_mov_b32_e32 v195, 0
	v_lshlrev_b32_e32 v42, 4, v0
	v_mov_b32_e32 v43, v195
	s_movk_i32 s20, 0x2000
	v_lshl_add_u64 v[10:11], s[34:35], 0, v[42:43]
	v_add_co_u32_e32 v20, vcc, s20, v10
	s_movk_i32 s42, 0x4000
	s_nop 0
	v_addc_co_u32_e32 v21, vcc, 0, v11, vcc
	v_lshlrev_b32_e32 v6, 6, v0
	v_add_co_u32_e32 v22, vcc, s42, v10
	s_movk_i32 s43, 0x6000
	v_and_b32_e32 v6, 0x7e00, v6
	v_mov_b32_e32 v7, v195
	v_addc_co_u32_e32 v23, vcc, 0, v11, vcc
	s_mov_b32 s5, 0
	global_load_dwordx4 v[2:5], v42, s[34:35]
	v_mov_b32_e32 v9, v195
	v_lshl_add_u64 v[12:13], s[18:19], 0, v[6:7]
	v_or_b32_e32 v8, 0x8000, v6
	v_lshl_add_u64 v[6:7], s[22:23], 0, v[6:7]
	v_add_co_u32_e32 v24, vcc, s43, v10
	global_load_dwordx4 v[118:121], v194, s[40:41]
	global_load_dwordx4 v[114:117], v194, s[40:41] offset:64
	v_addc_co_u32_e32 v25, vcc, 0, v11, vcc
	v_lshl_add_u64 v[26:27], v[12:13], 0, s[4:5]
	v_lshl_add_u64 v[28:29], s[18:19], 0, v[8:9]
	v_lshl_add_u64 v[30:31], v[6:7], 0, s[4:5]
	v_lshl_add_u64 v[32:33], s[22:23], 0, v[8:9]
	global_load_dwordx4 v[6:9], v[20:21], off
	global_load_dwordx4 v[10:13], v[22:23], off
	global_load_dwordx4 v[14:17], v[24:25], off
	v_and_b32_e32 v18, 0x70, v42
	v_mov_b32_e32 v19, v195
	v_lshl_add_u64 v[38:39], v[26:27], 0, v[18:19]
	v_lshl_add_u64 v[20:21], v[28:29], 0, s[4:5]
	v_lshl_add_u64 v[22:23], v[32:33], 0, s[4:5]
	v_lshl_add_u64 v[40:41], v[30:31], 0, v[18:19]
	global_load_dwordx4 v[126:129], v194, s[6:7]
	global_load_dwordx4 v[122:125], v194, s[6:7] offset:64
	v_lshl_add_u64 v[44:45], v[20:21], 0, v[18:19]
	v_lshl_add_u64 v[46:47], v[22:23], 0, v[18:19]
	global_load_dwordx4 v[18:21], v[38:39], off
	global_load_dwordx4 v[22:25], v[44:45], off
	global_load_dwordx4 v[26:29], v[40:41], off
	global_load_dwordx4 v[30:33], v[46:47], off
	s_movk_i32 s25, 0x2710
	s_add_i32 s20, s36, -2
	v_lshl_or_b32 v207, s20, 4, v199
	v_min_u32_e32 v43, 0xc7, v207
	v_and_b32_e32 v42, 48, v42
	v_lshlrev_b32_e32 v48, 2, v0
	s_waitcnt vmcnt(14)
	v_mad_u64_u32 v[34:35], s[4:5], v35, s25, v[34:35]
	v_ashrrev_i32_e32 v35, 31, v34
	v_lshlrev_b64 v[34:35], 9, v[34:35]
	s_waitcnt vmcnt(12)
	v_mad_u64_u32 v[36:37], s[4:5], v37, s25, v[36:37]
	v_ashrrev_i32_e32 v37, 31, v36
	v_lshlrev_b64 v[44:45], 9, v[36:37]
	v_lshl_add_u64 v[34:35], s[14:15], 0, v[34:35]
	v_lshl_add_u64 v[44:45], s[14:15], 0, v[44:45]
	v_lshl_add_u64 v[46:47], v[34:35], 0, v[194:195]
	v_lshl_add_u64 v[44:45], v[44:45], 0, v[194:195]
	global_load_dwordx4 v[34:37], v[46:47], off
	global_load_dwordx4 v[38:41], v[46:47], off offset:64
	global_load_dwordx4 v[54:57], v[46:47], off offset:128
	global_load_dwordx4 v[82:85], v[46:47], off offset:192
	global_load_dwordx4 v[86:89], v[46:47], off offset:256
	global_load_dwordx4 v[90:93], v[46:47], off offset:320
	global_load_dwordx4 v[94:97], v[46:47], off offset:384
	global_load_dwordx4 v[98:101], v[46:47], off offset:448
	global_load_dwordx4 v[158:161], v[44:45], off
	global_load_dwordx4 v[154:157], v[44:45], off offset:64
	global_load_dwordx4 v[150:153], v[44:45], off offset:128
	global_load_dwordx4 v[146:149], v[44:45], off offset:192
	global_load_dwordx4 v[66:69], v[44:45], off offset:256
	global_load_dwordx4 v[70:73], v[44:45], off offset:320
	global_load_dwordx4 v[74:77], v[44:45], off offset:384
	global_load_dwordx4 v[78:81], v[44:45], off offset:448
	v_add_u32_e32 v44, s37, v43
	v_ashrrev_i32_e32 v45, 31, v44
	v_lshlrev_b64 v[44:45], 2, v[44:45]
	v_lshl_add_u64 v[46:47], s[8:9], 0, v[44:45]
	v_lshl_add_u64 v[44:45], s[10:11], 0, v[44:45]
	global_load_dword v140, v[46:47], off
	global_load_dword v135, v[44:45], off
	v_min_u32_e32 v43, 0xc7, v204
	v_add_u32_e32 v44, s37, v43
	v_ashrrev_i32_e32 v45, 31, v44
	s_add_i32 s4, s24, 0x80
	v_lshlrev_b64 v[44:45], 2, v[44:45]
	v_or_b32_e32 v43, s4, v199
	v_lshl_add_u64 v[46:47], s[8:9], 0, v[44:45]
	v_lshl_add_u64 v[44:45], s[10:11], 0, v[44:45]
	v_min_u32_e32 v43, 0xc7, v43
	global_load_dword v133, v[44:45], off
	v_add_u32_e32 v44, s37, v43
	v_ashrrev_i32_e32 v45, 31, v44
	v_lshlrev_b64 v[44:45], 2, v[44:45]
	global_load_dword v130, v[46:47], off
	v_lshl_add_u64 v[46:47], s[8:9], 0, v[44:45]
	v_lshl_add_u64 v[44:45], s[10:11], 0, v[44:45]
	global_load_dword v134, v[44:45], off
	v_lshlrev_b32_e32 v45, 3, v0
	v_lshrrev_b32_e32 v43, 5, v0
	v_and_b32_e32 v44, 4, v0
	v_and_b32_e32 v45, 0xc0, v45
	v_or3_b32 v42, v42, v43, v45
	v_lshlrev_b32_e32 v43, 1, v44
	s_waitcnt vmcnt(32)
	v_cvt_pk_f16_f32 v2, v2, v3
	v_cvt_pk_f16_f32 v3, v4, v5
	v_lshl_or_b32 v42, v42, 4, v43
	s_waitcnt vmcnt(29)
	v_cvt_pk_f16_f32 v4, v6, v7
	v_cvt_pk_f16_f32 v5, v8, v9
	ds_write2st64_b64 v42, v[2:3], v[4:5] offset0:101 offset1:109
	s_waitcnt vmcnt(28)
	v_cvt_pk_f16_f32 v2, v10, v11
	v_cvt_pk_f16_f32 v3, v12, v13
	s_waitcnt vmcnt(27)
	v_cvt_pk_f16_f32 v4, v14, v15
	v_cvt_pk_f16_f32 v5, v16, v17
	ds_write2st64_b64 v42, v[2:3], v[4:5] offset0:117 offset1:125
	v_lshrrev_b32_e32 v4, 2, v0
	v_lshrrev_b32_e32 v2, 1, v0
	v_lshrrev_b32_e32 v3, 4, v0
	v_and_b32_e32 v4, 6, v4
	v_and_b32_e32 v2, 48, v2
	v_and_or_b32 v3, v3, 8, v4
	v_lshrrev_b32_e32 v4, 8, v0
	v_and_or_b32 v2, v48, 12, v2
	v_or_b32_e32 v4, v4, v44
	s_waitcnt vmcnt(24)
	v_cvt_f16_f32_e32 v5, v18
	v_lshlrev_b32_e32 v4, 10, v4
	v_lshlrev_b32_e32 v2, 4, v2
	v_or3_b32 v2, v2, v4, v3
	v_cvt_f16_f32_e32 v3, v19
	v_cvt_f16_f32_e32 v4, v20
	v_add_u32_e32 v2, 0x10a00, v2
	v_cvt_f16_f32_e32 v6, v21
	global_load_dword v132, v[46:47], off
	ds_write_b16 v2, v5
	ds_write_b16 v2, v3 offset:16
	ds_write_b16 v2, v4 offset:32
	ds_write_b16 v2, v6 offset:48
	s_waitcnt vmcnt(24)
	v_cvt_f16_f32_e32 v3, v22
	v_cvt_f16_f32_e32 v4, v23
	v_cvt_f16_f32_e32 v5, v24
	v_cvt_f16_f32_e32 v6, v25
	ds_write_b16 v2, v3 offset:2048
	ds_write_b16 v2, v4 offset:2064
	ds_write_b16 v2, v5 offset:2080
	ds_write_b16 v2, v6 offset:2096
	s_waitcnt vmcnt(23)
	v_cvt_f16_f32_e32 v3, v26
	v_cvt_f16_f32_e32 v4, v27
	v_cvt_f16_f32_e32 v5, v28
	v_cvt_f16_f32_e32 v6, v29
	ds_write_b16 v2, v3 offset:8192
	ds_write_b16 v2, v4 offset:8208
	ds_write_b16 v2, v5 offset:8224
	ds_write_b16 v2, v6 offset:8240
	s_waitcnt vmcnt(22)
	v_cvt_f16_f32_e32 v3, v30
	v_cvt_f16_f32_e32 v4, v31
	v_cvt_f16_f32_e32 v5, v32
	v_cvt_f16_f32_e32 v6, v33
	ds_write_b16 v2, v3 offset:10240
	ds_write_b16 v2, v4 offset:10256
	ds_write_b16 v2, v5 offset:10272
	ds_write_b16 v2, v6 offset:10288
	v_mov_b32_e32 v2, 0x10a00
	s_waitcnt lgkmcnt(0)
	s_barrier
	s_setprio 0
	v_lshl_add_u32 v141, v1, 4, v2
	ds_read_b128 v[6:9], v141
	ds_read_b128 v[2:5], v141 offset:1024
	ds_read_b128 v[10:13], v141 offset:4096
	ds_read_b128 v[14:17], v141 offset:8192
	s_waitcnt vmcnt(21)
	v_cvt_pk_f16_f32 v102, v34, v35
	v_cvt_pk_f16_f32 v103, v36, v37
	s_waitcnt vmcnt(20)
	v_cvt_pk_f16_f32 v104, v38, v39
	v_cvt_pk_f16_f32 v105, v40, v41
	ds_read_b128 v[26:29], v141 offset:2048
	ds_read_b128 v[18:21], v141 offset:3072
	ds_read_b128 v[46:49], v141 offset:5120
	ds_read_b128 v[58:61], v141 offset:12288
	s_waitcnt lgkmcnt(7)
	v_mfma_f32_16x16x32_f16 v[38:41], v[6:9], v[102:105], 0
	s_waitcnt vmcnt(19)
	v_cvt_pk_f16_f32 v136, v54, v55
	v_cvt_pk_f16_f32 v137, v56, v57
	s_waitcnt vmcnt(18)
	v_cvt_pk_f16_f32 v138, v82, v83
	s_waitcnt lgkmcnt(5)
	v_mfma_f32_16x16x32_f16 v[106:109], v[10:13], v[102:105], 0
	v_cvt_pk_f16_f32 v139, v84, v85
	ds_read_b128 v[34:37], v141 offset:6144
	ds_read_b128 v[22:25], v141 offset:7168
	ds_read_b128 v[50:53], v141 offset:9216
	ds_read_b128 v[42:45], v141 offset:10240
	ds_read_b128 v[30:33], v141 offset:11264
	ds_read_b128 v[62:65], v141 offset:13312
	v_mfma_f32_16x16x32_f16 v[82:85], v[2:5], v[136:139], v[38:41]
	ds_read_b128 v[54:57], v141 offset:14336
	s_nop 1
	ds_read_b128 v[38:41], v141 offset:15360
	s_waitcnt vmcnt(4)
	v_mad_u64_u32 v[144:145], s[4:5], v135, s25, v[140:141]
	s_waitcnt lgkmcnt(12)
	v_mfma_f32_16x16x32_f16 v[110:113], v[14:17], v[102:105], 0
	v_cvt_pk_f16_f32 v140, v86, v87
	v_cvt_pk_f16_f32 v141, v88, v89
	v_cvt_pk_f16_f32 v142, v90, v91
	s_waitcnt lgkmcnt(8)
	v_mfma_f32_16x16x32_f16 v[102:105], v[58:61], v[102:105], 0
	v_cvt_pk_f16_f32 v143, v92, v93
	v_cvt_pk_f16_f32 v164, v98, v99
	v_cvt_pk_f16_f32 v165, v100, v101
	v_mfma_f32_16x16x32_f16 v[106:109], v[46:49], v[136:139], v[106:109]
	s_add_i32 s4, s24, 0xa0
	v_ashrrev_i32_e32 v145, 31, v144
	v_cvt_pk_f16_f32 v162, v94, v95
	v_mfma_f32_16x16x32_f16 v[98:101], v[26:29], v[140:143], v[82:85]
	v_cvt_pk_f16_f32 v163, v96, v97
	s_waitcnt lgkmcnt(5)
	v_mfma_f32_16x16x32_f16 v[86:89], v[50:53], v[136:139], v[110:113]
	v_lshlrev_b64 v[82:83], 9, v[144:145]
	v_lshl_add_u64 v[82:83], s[14:15], 0, v[82:83]
	v_lshl_add_u64 v[94:95], v[82:83], 0, v[194:195]
	s_waitcnt lgkmcnt(2)
	v_mfma_f32_16x16x32_f16 v[102:105], v[62:65], v[136:139], v[102:105]
	global_load_dwordx4 v[190:193], v[94:95], off
	global_load_dwordx4 v[186:189], v[94:95], off offset:64
	global_load_dwordx4 v[182:185], v[94:95], off offset:128
	global_load_dwordx4 v[178:181], v[94:95], off offset:192
	v_mfma_f32_16x16x32_f16 v[110:113], v[34:37], v[140:143], v[106:109]
	s_nop 2
	v_or_b32_e32 v106, s4, v199
	v_min_u32_e32 v135, 0xc7, v106
	v_mfma_f32_16x16x32_f16 v[106:109], v[18:21], v[162:165], v[98:101]
	s_movk_i32 s4, 0xc8
	v_cmp_gt_u32_e32 vcc, s4, v131
	s_nop 0
	v_add_u32_e32 v98, s37, v135
	v_ashrrev_i32_e32 v99, 31, v98
	v_mfma_f32_16x16x32_f16 v[136:139], v[42:45], v[140:143], v[86:89]
	global_load_dwordx4 v[82:85], v[94:95], off offset:256
	s_nop 1
	global_load_dwordx4 v[86:89], v[94:95], off offset:320
	global_load_dwordx4 v[90:93], v[94:95], off offset:384
	s_nop 0
	global_load_dwordx4 v[94:97], v[94:95], off offset:448
	s_waitcnt lgkmcnt(1)
	v_mfma_f32_16x16x32_f16 v[102:105], v[54:57], v[140:143], v[102:105]
	v_lshlrev_b64 v[140:141], 2, v[98:99]
	v_mfma_f32_16x16x32_f16 v[98:101], v[22:25], v[162:165], v[110:113]
	s_nop 2
	v_lshl_add_u64 v[110:111], s[8:9], 0, v[140:141]
	v_lshl_add_u64 v[140:141], s[10:11], 0, v[140:141]
	global_load_dword v200, v[110:111], off
	global_load_dword v208, v[140:141], off
	v_mfma_f32_16x16x32_f16 v[110:113], v[30:33], v[162:165], v[136:139]
	s_waitcnt lgkmcnt(0)
	v_mfma_f32_16x16x32_f16 v[102:105], v[38:41], v[162:165], v[102:105]
	s_and_saveexec_b64 s[4:5], vcc
	s_cbranch_execz .LBB0_6
	v_mul_f32_e32 v135, 0xbfb8aa3b, v118
	v_fmac_f32_e32 v135, 0xbfb8aa3b, v106
	v_exp_f32_e32 v106, v135
	v_mul_f32_e32 v135, 0x4038aa3b, v126
	v_fmac_f32_e32 v135, 0x4038aa3b, v110
	v_exp_f32_e32 v110, v135
	v_add_f32_e32 v106, 1.0, v106
	v_rcp_f32_e32 v135, v106
	s_movk_i32 s6, 0xca0
	v_add_f32_e32 v106, 1.0, v110
	v_mul_f32_e32 v110, 0xbfb8aa3b, v114
	v_fmac_f32_e32 v110, 0xbfb8aa3b, v98
	v_exp_f32_e32 v98, v110
	v_mul_f32_e32 v110, 0x4038aa3b, v122
	v_fmac_f32_e32 v110, 0x4038aa3b, v102
	v_exp_f32_e32 v102, v110
	v_add_f32_e32 v98, 1.0, v98
	v_rcp_f32_e32 v110, v98
	v_rcp_f32_e32 v106, v106
	v_add_f32_e32 v98, 1.0, v102
	v_mul_f32_e32 v102, 0xbfb8aa3b, v119
	v_fmac_f32_e32 v102, 0xbfb8aa3b, v107
	v_mul_f32_e32 v107, 0x4038aa3b, v127
	v_exp_f32_e32 v102, v102
	v_fmac_f32_e32 v107, 0x4038aa3b, v111
	v_exp_f32_e32 v107, v107
	v_rcp_f32_e32 v98, v98
	v_add_f32_e32 v102, 1.0, v102
	v_rcp_f32_e32 v111, v102
	v_add_f32_e32 v102, 1.0, v107
	v_rcp_f32_e32 v107, v102
	v_mul_f32_e32 v102, 0xbfb8aa3b, v115
	v_fmac_f32_e32 v102, 0xbfb8aa3b, v99
	v_exp_f32_e32 v99, v102
	v_mul_f32_e32 v102, 0x4038aa3b, v123
	v_fmac_f32_e32 v102, 0x4038aa3b, v103
	v_exp_f32_e32 v136, v102
	v_pk_fma_f32 v[102:103], v[106:107], -2.0, 1.0 op_sel_hi:[1,0,0]
	v_mul_f32_e32 v106, 0xbfb8aa3b, v120
	v_fmac_f32_e32 v106, 0xbfb8aa3b, v108
	v_mul_f32_e32 v107, 0x4038aa3b, v128
	v_exp_f32_e32 v106, v106
	v_fmac_f32_e32 v107, 0x4038aa3b, v112
	v_exp_f32_e32 v107, v107
	v_add_f32_e32 v99, 1.0, v99
	v_add_f32_e32 v106, 1.0, v106
	v_rcp_f32_e32 v108, v106
	v_add_f32_e32 v106, 1.0, v107
	v_mul_f32_e32 v107, 0xbfb8aa3b, v116
	v_fmac_f32_e32 v107, 0xbfb8aa3b, v100
	v_exp_f32_e32 v100, v107
	v_mul_f32_e32 v107, 0x4038aa3b, v124
	v_fmac_f32_e32 v107, 0x4038aa3b, v104
	v_exp_f32_e32 v104, v107
	v_add_f32_e32 v100, 1.0, v100
	v_rcp_f32_e32 v112, v100
	v_mul_f32_e32 v107, 0x4038aa3b, v129
	v_add_f32_e32 v100, 1.0, v104
	v_mul_f32_e32 v104, 0xbfb8aa3b, v121
	v_fmac_f32_e32 v104, 0xbfb8aa3b, v109
	v_exp_f32_e32 v104, v104
	v_fmac_f32_e32 v107, 0x4038aa3b, v113
	v_exp_f32_e32 v107, v107
	v_rcp_f32_e32 v106, v106
	v_add_f32_e32 v104, 1.0, v104
	v_rcp_f32_e32 v109, v104
	v_add_f32_e32 v104, 1.0, v107
	v_rcp_f32_e32 v107, v104
	v_mul_f32_e32 v104, 0x4038aa3b, v125
	v_fmac_f32_e32 v104, 0x4038aa3b, v105
	v_mul_f32_e32 v105, 0xbfb8aa3b, v117
	v_exp_f32_e32 v104, v104
	v_fmac_f32_e32 v105, 0xbfb8aa3b, v101
	v_exp_f32_e32 v113, v105
	v_rcp_f32_e32 v137, v99
	v_add_f32_e32 v99, 1.0, v136
	v_add_f32_e32 v101, 1.0, v104
	v_rcp_f32_e32 v99, v99
	v_rcp_f32_e32 v100, v100
	v_rcp_f32_e32 v101, v101
	v_pk_fma_f32 v[104:105], v[106:107], -2.0, 1.0 op_sel_hi:[1,0,0]
	v_add_f32_e32 v106, 1.0, v113
	v_rcp_f32_e32 v113, v106
	v_cvt_pk_f16_f32 v107, v102, v103
	v_lshlrev_b32_e32 v102, 3, v131
	v_cvt_pk_f16_f32 v106, v135, v111
	v_mad_u32_u24 v111, v206, s6, v102
	v_pk_fma_f32 v[98:99], v[98:99], -2.0, 1.0 op_sel_hi:[1,0,0]
	v_pk_fma_f32 v[100:101], v[100:101], -2.0, 1.0 op_sel_hi:[1,0,0]
	v_cvt_pk_f16_f32 v102, v108, v109
	v_cvt_pk_f16_f32 v103, v104, v105
	v_add_u32_e32 v104, 0x6400, v111
	ds_write2_b64 v104, v[106:107], v[102:103] offset0:32 offset1:234
	v_cvt_pk_f16_f32 v102, v110, v137
	v_cvt_pk_f16_f32 v103, v98, v99
	v_cvt_pk_f16_f32 v98, v112, v113
	v_cvt_pk_f16_f32 v99, v100, v101
	v_add_u32_e32 v100, 0x9600, v111
	ds_write2_b64 v100, v[102:103], v[98:99] offset0:48 offset1:250

.LBB0_52:
	s_and_b64 vcc, exec, s[4:5]
	s_cbranch_vccz .LBB0_77
	s_add_i32 s42, s36, -4
	s_waitcnt vmcnt(2)
	v_lshl_or_b32 v87, s42, 4, v199
	s_waitcnt lgkmcnt(0)
	s_add_i32 s24, s36, -2
	v_add_u32_e32 v2, s37, v87
	v_lshl_or_b32 v179, s24, 4, v199
	v_ashrrev_i32_e32 v3, 31, v2
	v_add_u32_e32 v6, s37, v179
	v_lshl_add_u64 v[4:5], v[2:3], 2, s[8:9]
	v_ashrrev_i32_e32 v7, 31, v6
	v_lshl_add_u64 v[6:7], v[6:7], 2, s[8:9]
	global_load_dword v36, v[4:5], off
	global_load_dword v38, v[6:7], off
	v_lshlrev_b32_e32 v40, 4, v0
	v_mov_b32_e32 v41, 0
	s_movk_i32 s4, 0x2000
	v_lshl_add_u64 v[16:17], s[34:35], 0, v[40:41]
	v_add_co_u32_e32 v18, vcc, s4, v16
	s_movk_i32 s5, 0x4000
	s_nop 0
	v_addc_co_u32_e32 v19, vcc, 0, v17, vcc
	v_add_u32_e32 v4, s37, v204
	v_add_co_u32_e32 v20, vcc, s5, v16
	s_movk_i32 s6, 0x6000
	v_ashrrev_i32_e32 v5, 31, v4
	v_addc_co_u32_e32 v21, vcc, 0, v17, vcc
	v_lshl_add_u64 v[8:9], v[4:5], 2, s[8:9]
	v_add_co_u32_e32 v16, vcc, s6, v16
	global_load_dword v42, v[8:9], off
	global_load_dwordx4 v[4:7], v40, s[34:35]
	v_addc_co_u32_e32 v17, vcc, 0, v17, vcc
	global_load_dwordx4 v[8:11], v[18:19], off
	global_load_dwordx4 v[12:15], v[20:21], off
	v_lshlrev_b32_e32 v3, 6, v0
	global_load_dwordx4 v[16:19], v[16:17], off
	v_and_b32_e32 v24, 0x7e00, v3
	v_mov_b32_e32 v25, v41
	s_mov_b32 s5, 0
	s_lshl_b32 s4, s33, 7
	v_lshl_add_u64 v[20:21], s[18:19], 0, v[24:25]
	v_and_b32_e32 v28, 0x70, v40
	v_mov_b32_e32 v29, v41
	v_lshl_add_u64 v[20:21], v[20:21], 0, s[4:5]
	v_lshl_add_u64 v[20:21], v[20:21], 0, v[28:29]
	global_load_dwordx4 v[20:23], v[20:21], off
	v_mov_b32_e32 v27, v41
	v_or_b32_e32 v26, 0x8000, v24
	v_lshl_add_u64 v[24:25], s[22:23], 0, v[24:25]
	v_lshl_add_u64 v[30:31], s[18:19], 0, v[26:27]
	v_lshl_add_u64 v[32:33], v[24:25], 0, s[4:5]
	v_lshl_add_u64 v[24:25], v[30:31], 0, s[4:5]
	v_lshl_add_u64 v[24:25], v[24:25], 0, v[28:29]
	v_lshl_add_u64 v[34:35], s[22:23], 0, v[26:27]
	global_load_dwordx4 v[24:27], v[24:25], off
	v_lshl_add_u64 v[44:45], v[32:33], 0, v[28:29]
	v_lshl_add_u64 v[30:31], v[34:35], 0, s[4:5]
	v_lshl_add_u64 v[46:47], v[30:31], 0, v[28:29]
	global_load_dwordx4 v[28:31], v[44:45], off
	global_load_dwordx4 v[32:35], v[46:47], off
	s_add_i32 s39, s36, 2
	s_waitcnt vmcnt(11)
	v_mov_b32_e32 v195, v41
	s_lshl_b32 s41, s39, 4
	s_add_i32 s4, s41, s37
	v_lshlrev_b32_e32 v3, 2, v0
	s_load_dwordx2 s[20:21], s[0:1], 0x70
	s_cmp_eq_u32 s33, 0
	s_waitcnt vmcnt(10)
	v_ashrrev_i32_e32 v37, 31, v36
	s_waitcnt vmcnt(9)
	v_ashrrev_i32_e32 v39, 31, v38
	v_lshlrev_b64 v[36:37], 9, v[36:37]
	v_lshlrev_b64 v[38:39], 9, v[38:39]
	v_lshl_add_u64 v[36:37], s[12:13], 0, v[36:37]
	v_lshl_add_u64 v[38:39], s[12:13], 0, v[38:39]
	v_lshl_add_u64 v[36:37], v[36:37], 0, v[194:195]
	v_lshl_add_u64 v[38:39], v[38:39], 0, v[194:195]
	global_load_dwordx4 v[66:69], v[36:37], off
	global_load_dwordx4 v[70:73], v[36:37], off offset:64
	global_load_dwordx4 v[74:77], v[36:37], off offset:128
	global_load_dwordx4 v[102:105], v[36:37], off offset:192
	global_load_dwordx4 v[110:113], v[36:37], off offset:256
	global_load_dwordx4 v[162:165], v[36:37], off offset:320
	global_load_dwordx4 v[166:169], v[36:37], off offset:384
	global_load_dwordx4 v[170:173], v[36:37], off offset:448
	global_load_dwordx4 v[142:145], v[38:39], off
	global_load_dwordx4 v[138:141], v[38:39], off offset:64
	global_load_dwordx4 v[134:137], v[38:39], off offset:128
	global_load_dwordx4 v[130:133], v[38:39], off offset:192
	global_load_dwordx4 v[122:125], v[38:39], off offset:256
	global_load_dwordx4 v[118:121], v[38:39], off offset:320
	global_load_dwordx4 v[90:93], v[38:39], off offset:384
	global_load_dwordx4 v[94:97], v[38:39], off offset:448
	v_add_u32_e32 v36, s4, v199
	v_add_u32_e32 v38, 0x80, v2
	v_ashrrev_i32_e32 v37, 31, v36
	v_ashrrev_i32_e32 v39, 31, v38
	v_lshl_add_u64 v[36:37], v[36:37], 2, s[8:9]
	v_lshl_add_u64 v[38:39], v[38:39], 2, s[8:9]
	global_load_dword v88, v[36:37], off
	global_load_dword v86, v[38:39], off
	v_lshlrev_b32_e32 v39, 3, v0
	v_lshrrev_b32_e32 v36, 5, v0
	v_and_b32_e32 v37, 4, v0
	v_and_b32_e32 v38, 48, v40
	v_and_b32_e32 v39, 0xc0, v39
	v_or3_b32 v36, v38, v36, v39
	v_lshlrev_b32_e32 v38, 1, v37
	s_waitcnt vmcnt(25)
	v_cvt_pk_f16_f32 v4, v4, v5
	v_cvt_pk_f16_f32 v5, v6, v7
	v_lshl_or_b32 v36, v36, 4, v38
	s_waitcnt vmcnt(24)
	v_cvt_pk_f16_f32 v6, v8, v9
	v_cvt_pk_f16_f32 v7, v10, v11
	ds_write2st64_b64 v36, v[4:5], v[6:7] offset0:101 offset1:109
	s_waitcnt vmcnt(23)
	v_cvt_pk_f16_f32 v4, v12, v13
	v_cvt_pk_f16_f32 v5, v14, v15
	s_waitcnt vmcnt(22)
	v_cvt_pk_f16_f32 v6, v16, v17
	v_cvt_pk_f16_f32 v7, v18, v19
	ds_write2st64_b64 v36, v[4:5], v[6:7] offset0:117 offset1:125
	v_lshrrev_b32_e32 v4, 1, v0
	v_and_b32_e32 v4, 48, v4
	v_lshrrev_b32_e32 v5, 2, v0
	v_and_or_b32 v3, v3, 12, v4
	v_lshrrev_b32_e32 v4, 4, v0
	v_and_b32_e32 v5, 6, v5
	v_and_or_b32 v4, v4, 8, v5
	v_lshrrev_b32_e32 v5, 8, v0
	v_or_b32_e32 v5, v5, v37
	s_waitcnt vmcnt(21)
	v_cvt_f16_f32_e32 v6, v20
	v_lshlrev_b32_e32 v5, 10, v5
	v_lshlrev_b32_e32 v3, 4, v3
	v_or3_b32 v3, v3, v5, v4
	v_cvt_f16_f32_e32 v4, v21
	v_cvt_f16_f32_e32 v5, v22
	v_add_u32_e32 v3, 0x10a00, v3
	v_cvt_f16_f32_e32 v7, v23
	ds_write_b16 v3, v6
	ds_write_b16 v3, v4 offset:16
	ds_write_b16 v3, v5 offset:32
	ds_write_b16 v3, v7 offset:48
	s_waitcnt vmcnt(20)
	v_cvt_f16_f32_e32 v4, v24
	v_cvt_f16_f32_e32 v5, v25
	v_cvt_f16_f32_e32 v6, v26
	v_cvt_f16_f32_e32 v7, v27
	ds_write_b16 v3, v4 offset:2048
	ds_write_b16 v3, v5 offset:2064
	ds_write_b16 v3, v6 offset:2080
	ds_write_b16 v3, v7 offset:2096
	s_waitcnt vmcnt(19)
	v_cvt_f16_f32_e32 v4, v28
	v_cvt_f16_f32_e32 v5, v29
	v_cvt_f16_f32_e32 v6, v30
	v_cvt_f16_f32_e32 v7, v31
	ds_write_b16 v3, v4 offset:8192
	ds_write_b16 v3, v5 offset:8208
	ds_write_b16 v3, v6 offset:8224
	ds_write_b16 v3, v7 offset:8240
	s_waitcnt vmcnt(18)
	v_cvt_f16_f32_e32 v4, v32
	v_cvt_f16_f32_e32 v5, v33
	v_cvt_f16_f32_e32 v6, v34
	v_ashrrev_i32_e32 v43, 31, v42
	v_cvt_f16_f32_e32 v7, v35
	ds_write_b16 v3, v4 offset:10240
	ds_write_b16 v3, v5 offset:10256
	ds_write_b16 v3, v6 offset:10272
	ds_write_b16 v3, v7 offset:10288
	v_lshlrev_b64 v[4:5], 9, v[42:43]
	v_lshl_add_u64 v[4:5], s[12:13], 0, v[4:5]
	s_waitcnt lgkmcnt(0)
	s_barrier
	s_setprio 0
	v_lshl_add_u64 v[4:5], v[4:5], 0, v[194:195]
	global_load_dwordx4 v[158:161], v[4:5], off
	global_load_dwordx4 v[154:157], v[4:5], off offset:64
	global_load_dwordx4 v[150:153], v[4:5], off offset:128
	global_load_dwordx4 v[146:149], v[4:5], off offset:192
	global_load_dwordx4 v[126:129], v[4:5], off offset:256
	global_load_dwordx4 v[114:117], v[4:5], off offset:320
	global_load_dwordx4 v[106:109], v[4:5], off offset:384
	global_load_dwordx4 v[98:101], v[4:5], off offset:448
	v_add_u32_e32 v2, 0xa0, v2
	v_ashrrev_i32_e32 v3, 31, v2
	v_lshl_add_u64 v[2:3], v[2:3], 2, s[8:9]
	global_load_dword v178, v[2:3], off
	v_lshlrev_b32_e32 v10, 4, v1
	v_add_u32_e32 v11, 0xca00, v10
	ds_read_b128 v[30:33], v10 offset:51712
	ds_read_b128 v[22:25], v10 offset:52736
	ds_read_b128 v[18:21], v10 offset:53760
	ds_read_b128 v[14:17], v10 offset:54784
	ds_read_b128 v[46:49], v10 offset:55808
	ds_read_b128 v[34:37], v10 offset:56832
	ds_read_b128 v[26:29], v10 offset:57856
	ds_read_b128 v[2:5], v10 offset:58880
	ds_read_b128 v[54:57], v10 offset:59904
	ds_read_b128 v[50:53], v10 offset:60928
	ds_read_b128 v[38:41], v10 offset:61952
	ds_read_b128 v[6:9], v10 offset:62976
	ds_read_b128 v[62:65], v10 offset:64000
	ds_read_b128 v[58:61], v10 offset:65024
	ds_read_b128 v[42:45], v11 offset:14336
	ds_read_b128 v[10:13], v11 offset:15360
	s_waitcnt vmcnt(26)
	v_cvt_pk_f16_f32 v82, v66, v67
	v_cvt_pk_f16_f32 v83, v68, v69
	s_waitcnt vmcnt(25)
	v_cvt_pk_f16_f32 v84, v70, v71
	v_cvt_pk_f16_f32 v85, v72, v73
	s_cselect_b64 s[4:5], -1, 0
	s_cmp_lg_u32 s33, 0
	v_mov_b64_e32 v[66:67], v[82:83]
	s_waitcnt vmcnt(24)
	v_cvt_pk_f16_f32 v78, v74, v75
	v_cvt_pk_f16_f32 v79, v76, v77
	s_waitcnt vmcnt(23)
	v_cvt_pk_f16_f32 v80, v102, v103
	v_cvt_pk_f16_f32 v81, v104, v105
	s_waitcnt vmcnt(22)
	v_cvt_pk_f16_f32 v74, v110, v111
	v_cvt_pk_f16_f32 v75, v112, v113
	s_waitcnt vmcnt(21)
	v_cvt_pk_f16_f32 v76, v162, v163
	v_cvt_pk_f16_f32 v77, v164, v165
	s_waitcnt vmcnt(20)
	v_cvt_pk_f16_f32 v70, v166, v167
	v_cvt_pk_f16_f32 v71, v168, v169
	s_waitcnt vmcnt(19)
	v_cvt_pk_f16_f32 v72, v170, v171
	v_cvt_pk_f16_f32 v73, v172, v173
	s_cselect_b64 s[10:11], -1, 0
	s_and_b64 vcc, exec, s[4:5]
	v_mov_b64_e32 v[68:69], v[84:85]
	s_cbranch_vccnz .LBB0_55
	s_cmp_eq_u32 s33, 1
	s_cselect_b64 vcc, -1, 0
	s_cmp_eq_u32 s33, 2
	s_cselect_b64 s[6:7], -1, 0
	v_cndmask_b32_e64 v66, v70, v74, s[6:7]
	v_cndmask_b32_e64 v67, v71, v75, s[6:7]
	v_cndmask_b32_e64 v68, v72, v76, s[6:7]
	v_cndmask_b32_e64 v69, v73, v77, s[6:7]
	v_cndmask_b32_e32 v69, v69, v81, vcc
	v_cndmask_b32_e32 v68, v68, v80, vcc
	v_cndmask_b32_e32 v67, v67, v79, vcc
	v_cndmask_b32_e32 v66, v66, v78, vcc
